# combo7 + wave stagger in attention: waves 4-7 sleep 1280 cycles once per unit after the staging barrier
# speedup vs baseline: 1.0011x; 1.0011x over previous
.LBB0_558:
	s_or_b64 exec, exec, s[10:11]
	s_waitcnt vmcnt(1)
	ds_write_b128 v81, v[2:5] offset:36864
	s_waitcnt vmcnt(0)
	ds_write_b128 v82, v[6:9] offset:36864
	v_lshlrev_b32_e32 v2, 2, v64
	v_lshl_or_b32 v2, s5, 4, v2
	s_waitcnt lgkmcnt(0)
	s_barrier
	v_readfirstlane_b32 s22, v0
	s_bitcmp0_b32 s22, 8
	s_cbranch_scc1 .Lstag_attn_skip
	s_sleep 20
.Lstag_attn_skip:
	global_load_dword v53, v2, s[6:7]
	s_lshr_b32 s5, s14, 4
	s_and_b32 s5, s5, 3
	s_lshl_b32 s10, s5, 9
	s_ashr_i32 s5, s4, 31
	s_and_b32 s8, s18, 0x780
	s_lshl_b64 s[4:5], s[4:5], 11
	v_or_b32_e32 v42, s8, v1
	v_mov_b32_e32 v3, s5
	v_or_b32_e32 v2, s4, v48
	v_lshl_add_u64 v[2:3], v[2:3], 0, v[42:43]
	v_lshlrev_b64 v[2:3], 11, v[2:3]
	v_or3_b32 v2, s10, v80, v2
	s_sub_i32 s8, 0x7f, s21
	v_lshl_add_u64 v[60:61], v[46:47], 0, v[2:3]
	v_lshl_add_u64 v[62:63], v[50:51], 0, v[2:3]
	s_mov_b64 s[10:11], 0
	v_mov_b32_e32 v42, v75
	v_mov_b32_e32 v55, v74
